# attention fast path rewritten with v_mfma_f32_16x16x32_bf16 (was 32x32x16): new V^T LDS image, Q fragment re-layout via LDS, new epilogue; same bf16 operands and f32 accumulation
# speedup vs baseline: 1.0177x; 1.0161x over previous
.LBB0_733:
	s_or_b64 exec, exec, s[8:9]
	s_movk_i32 s4, 0xf0
	s_cmp_lg_u32 0, -1
	v_lshlrev_b32_e32 v39, 8, v141
	v_bitop3_b32 v80, v142, s4, v136 bitop3:0x48
	s_cselect_b32 s10, 0, 0
	v_cvt_pk_bf16_f32 v96, v134, v135
	v_cvt_pk_bf16_f32 v97, v132, v133
	v_cvt_pk_bf16_f32 v98, v130, v131
	v_cvt_pk_bf16_f32 v99, v128, v129
	v_cvt_pk_bf16_f32 v100, v126, v127
	v_cvt_pk_bf16_f32 v101, v124, v125
	v_cvt_pk_bf16_f32 v102, v122, v123
	v_cvt_pk_bf16_f32 v103, v120, v121
	v_cvt_pk_bf16_f32 v104, v70, v71
	v_cvt_pk_bf16_f32 v105, v74, v75
	v_cvt_pk_bf16_f32 v106, v64, v65
	v_cvt_pk_bf16_f32 v107, v68, v69
	v_cvt_pk_bf16_f32 v108, v60, v61
	v_cvt_pk_bf16_f32 v109, v66, v67
	v_cvt_pk_bf16_f32 v110, v56, v57
	v_cvt_pk_bf16_f32 v111, v58, v59
	v_cvt_pk_bf16_f32 v112, v112, v113
	v_cvt_pk_bf16_f32 v113, v118, v119
	v_cvt_pk_bf16_f32 v114, v114, v115
	v_cvt_pk_bf16_f32 v115, v116, v117
	v_cvt_pk_bf16_f32 v116, v78, v79
	v_cvt_pk_bf16_f32 v117, v76, v77
	v_cvt_pk_bf16_f32 v118, v72, v73
	v_cvt_pk_bf16_f32 v119, v62, v63
	v_cvt_pk_bf16_f32 v120, v52, v53
	v_cvt_pk_bf16_f32 v121, v54, v55
	v_cvt_pk_bf16_f32 v122, v46, v47
	v_cvt_pk_bf16_f32 v123, v50, v51
	v_cvt_pk_bf16_f32 v124, v44, v45
	v_cvt_pk_bf16_f32 v125, v48, v49
	v_cvt_pk_bf16_f32 v126, v40, v41
	v_cvt_pk_bf16_f32 v127, v42, v43
	v_readlane_b32 s100, v250, 8
	v_mbcnt_lo_u32_b32 v68, -1, 0
	v_mbcnt_hi_u32_b32 v68, -1, v68
	s_nop 1
	v_add_u32_e32 v69, s100, v68
	v_lshrrev_b32_e32 v70, 3, v69
	v_and_b32_e32 v71, 7, v69
	v_lshrrev_b32_e32 v72, 2, v71
	v_bfe_u32 v73, v71, 1, 1
	v_and_b32_e32 v74, 1, v71
	v_lshlrev_b32_e32 v74, 1, v74
	v_lshl_add_u32 v75, v72, 2, v74
	v_bfe_u32 v76, v70, 1, 3
	v_xor_b32_e32 v77, v75, v76
	v_add_u32_e32 v78, 1, v75
	v_xor_b32_e32 v78, v78, v76
	v_lshlrev_b32_e32 v79, 7, v70
	v_lshl_add_u32 v79, v73, 3, v79
	v_lshl_add_u32 v64, v77, 4, v79
	v_lshl_add_u32 v65, v78, 4, v79
	v_add_u32_e32 v66, 0x2000, v64
	v_add_u32_e32 v67, 0x2000, v65
	v_or_b32_e32 v81, v39, v80
	s_add_i32 s15, s10, 0x10000
	v_and_b32_e32 v82, 6, v137
	v_lshrrev_b32_e32 v84, 4, v136
	s_waitcnt vmcnt(0)
	s_waitcnt vmcnt(0)
	s_add_i32 s11, s10, 0x12000
	v_lshl_add_u32 v83, v139, 7, s10
	v_bitop3_b32 v85, v84, v82, 7 bitop3:0x6c
	v_and_b32_e32 v86, 8, v138
	v_or_b32_e32 v82, 1, v82
	v_add_u32_e32 v225, s15, v81
	s_waitcnt vmcnt(4)
	ds_write_b128 v225, v[24:27] offset:0
	v_lshlrev_b32_e32 v85, 4, v85
	v_add_u32_e32 v87, v83, v86
	v_bitop3_b32 v82, v84, v82, 7 bitop3:0x6c
	v_add3_u32 v226, v80, s11, v39
	ds_write_b128 v226, v[28:31] offset:0
	v_lshlrev_b32_e32 v82, 4, v82
	v_add_u32_e32 v227, v87, v85
	ds_write_b64 v64, v[12:13] offset:0
	v_lshrrev_b32_e32 v32, 5, v136
	v_add_u32_e32 v83, 0x2000, v83
	v_or_b32_e32 v84, v85, v86
	v_add_u32_e32 v228, v87, v82
	ds_write_b64 v65, v[14:15] offset:0
	v_xor_b32_e32 v32, v32, v137
	v_or_b32_e32 v86, v82, v86
	v_add_u32_e32 v229, v84, v83
	ds_write_b64 v66, v[4:5] offset:0
	v_lshlrev_b32_e32 v32, 4, v32
	v_add_u32_e32 v184, v86, v83
	ds_write_b64 v67, v[6:7] offset:0
	v_lshlrev_b32_e32 v33, 8, v143
	v_and_b32_e32 v32, 16, v32
	v_bfe_u32 v35, v137, 1, 3
	s_waitcnt vmcnt(4)
	ds_write_b128 v225, v[20:23] offset:0x4000
	v_lshlrev_b32_e32 v36, 5, v35
	v_add3_u32 v32, v33, s15, v32
	s_movk_i32 s16, 0x60
	ds_write_b128 v226, v[16:19] offset:0x4000
	v_xad_u32 v204, v36, s16, v32
	s_movk_i32 s16, 0x80
	ds_write_b64 v64, v[8:9] offset:0x4000
	v_xad_u32 v205, v36, s16, v32
	s_movk_i32 s16, 0xa0
	ds_write_b64 v65, v[10:11] offset:0x4000
	s_add_u32 s8, s6, 0x100
	v_xad_u32 v206, v36, s16, v32
	s_movk_i32 s16, 0xc0
	ds_write_b64 v66, v[0:1] offset:0x4000
	s_addc_u32 s9, s7, 0
	v_xad_u32 v207, v36, s16, v32
	s_movk_i32 s16, 0xe0
	ds_write_b64 v67, v[2:3] offset:0x4000
	v_add_u32_e32 v201, v32, v36
	v_xad_u32 v202, v36, 32, v32
	v_xad_u32 v203, v36, 64, v32
	v_xad_u32 v208, v36, s16, v32
	v_lshl_add_u32 v32, v143, 7, s10
	s_add_u32 s10, s78, 0x20000
	global_load_dwordx4 v[132:135], v198, s[8:9]
	s_addc_u32 s11, s79, 0
	global_load_dwordx4 v[128:131], v199, s[8:9]
	v_lshrrev_b32_e32 v34, 1, v137
	global_load_dwordx4 v[136:139], v196, s[10:11]
	s_add_u32 s6, s6, 0x180
	v_bitop3_b32 v34, v140, v34, 7 bitop3:0x78
	v_bitop3_b32 v37, v140, v35, 2 bitop3:0x36
	v_bitop3_b32 v38, v140, v35, 4 bitop3:0x36
	v_bitop3_b32 v35, v140, v35, 6 bitop3:0x36
	global_load_dwordx4 v[140:143], v197, s[10:11]
	s_addc_u32 s7, s7, 0
	s_add_u32 s8, s78, 0x30000
	global_load_dwordx4 v[148:151], v198, s[6:7]
	s_addc_u32 s9, s79, 0
	global_load_dwordx4 v[144:147], v199, s[6:7]
	global_load_dwordx4 v[152:155], v196, s[8:9]
	s_add_u32 s10, s13, s14
	global_load_dwordx4 v[156:159], v197, s[8:9]
	s_addc_u32 s11, s12, 0
	s_add_u32 s12, s41, s30
	v_mov_b32_e32 v0, 0
	s_mov_b32 s4, 0
	v_lshl_add_u32 v209, v34, 4, v32
	v_lshl_add_u32 v210, v37, 4, v32
	v_lshl_add_u32 v211, v38, 4, v32
	v_lshl_add_u32 v224, v35, 4, v32
	s_addc_u32 s13, 0, s31
	v_mov_b32_e32 v1, v0
	v_mov_b32_e32 v2, v0
	v_mov_b32_e32 v3, v0
	v_mov_b32_e32 v4, v0
	v_mov_b32_e32 v5, v0
	v_mov_b32_e32 v6, v0
	v_mov_b32_e32 v7, v0
	v_mov_b32_e32 v8, v0
	v_mov_b32_e32 v9, v0
	v_mov_b32_e32 v10, v0
	v_mov_b32_e32 v11, v0
	v_mov_b32_e32 v12, v0
	v_mov_b32_e32 v13, v0
	v_mov_b32_e32 v14, v0
	v_mov_b32_e32 v15, v0
	v_mov_b32_e32 v16, v0
	v_mov_b32_e32 v17, v0
	v_mov_b32_e32 v18, v0
	v_mov_b32_e32 v19, v0
	v_mov_b32_e32 v20, v0
	v_mov_b32_e32 v21, v0
	v_mov_b32_e32 v22, v0
	v_mov_b32_e32 v23, v0
	v_mov_b32_e32 v24, v0
	v_mov_b32_e32 v25, v0
	v_mov_b32_e32 v26, v0
	v_mov_b32_e32 v27, v0
	v_mov_b32_e32 v28, v0
	v_mov_b32_e32 v29, v0
	v_mov_b32_e32 v30, v0
	v_mov_b32_e32 v31, v0
	v_mov_b32_e32 v32, v0
	v_mov_b32_e32 v33, v0
	v_mov_b32_e32 v34, v0
	v_mov_b32_e32 v35, v0
	v_mov_b32_e32 v36, v0
	v_mov_b32_e32 v37, v0
	v_mov_b32_e32 v38, v0
	v_mov_b32_e32 v39, v0
	v_mov_b32_e32 v40, v0
	v_mov_b32_e32 v41, v0
	v_mov_b32_e32 v42, v0
	v_mov_b32_e32 v43, v0
	v_mov_b32_e32 v44, v0
	v_mov_b32_e32 v45, v0
	v_mov_b32_e32 v46, v0
	v_mov_b32_e32 v47, v0
	v_mov_b32_e32 v48, v0
	v_mov_b32_e32 v49, v0
	v_mov_b32_e32 v50, v0
	v_mov_b32_e32 v51, v0
	v_mov_b32_e32 v52, v0
	v_mov_b32_e32 v53, v0
	v_mov_b32_e32 v54, v0
	v_mov_b32_e32 v55, v0
	v_mov_b32_e32 v56, v0
	v_mov_b32_e32 v57, v0
	v_mov_b32_e32 v58, v0
	v_mov_b32_e32 v59, v0
	v_mov_b32_e32 v60, v0
	v_mov_b32_e32 v61, v0
	v_mov_b32_e32 v62, v0
	v_mov_b32_e32 v63, v0
	v_mov_b32_e32 v160, v0
	v_mov_b32_e32 v161, v0
	v_mov_b32_e32 v227, v64
	v_mov_b32_e32 v228, v65
	v_mov_b32_e32 v229, v66
	v_mov_b32_e32 v184, v67
	v_readlane_b32 s100, v250, 8
	v_mbcnt_lo_u32_b32 v68, -1, 0
	v_mbcnt_hi_u32_b32 v68, -1, v68
	v_and_b32_e32 v69, 15, v68
	v_lshrrev_b32_e32 v70, 4, v68
	v_lshlrev_b32_e32 v72, 8, v69
	v_add_u32_e32 v72, 0x10000, v72
	v_add_u32_e32 v71, 0, v70
	v_xor_b32_e32 v71, v71, v69
	v_lshl_add_u32 v201, v71, 4, v72
	v_add_u32_e32 v71, 4, v70
	v_xor_b32_e32 v71, v71, v69
	v_lshl_add_u32 v202, v71, 4, v72
	v_add_u32_e32 v71, 8, v70
	v_xor_b32_e32 v71, v71, v69
	v_lshl_add_u32 v203, v71, 4, v72
	v_add_u32_e32 v71, 12, v70
	v_xor_b32_e32 v71, v71, v69
	v_lshl_add_u32 v204, v71, 4, v72
	v_bfe_u32 v73, v69, 1, 3
	v_lshlrev_b32_e32 v76, 7, v69
	v_add_u32_e32 v71, 0, v70
	v_xor_b32_e32 v71, v71, v73
	v_lshl_add_u32 v209, v71, 4, v76
	v_add_u32_e32 v71, 4, v70
	v_xor_b32_e32 v71, v71, v73
	v_lshl_add_u32 v210, v71, 4, v76
	s_lshl_b32 s101, s100, 7
	s_add_u32 s101, s101, 0x8000
	s_cmpk_ge_u32 s100, 0x100
	s_cselect_b32 s6, 0x8000, 0
	s_add_u32 s101, s101, s6
	v_and_b32_e32 v74, 31, v68
	v_lshrrev_b32_e32 v75, 5, v68
	v_lshlrev_b32_e32 v74, 8, v74
	v_lshl_add_u32 v74, v75, 4, v74
	v_add_u32_e32 v74, s101, v74
	v_lshlrev_b32_e32 v75, 8, v69
	v_lshl_add_u32 v75, v70, 4, v75
	v_add_u32_e32 v75, s101, v75
	ds_write_b128 v74, v[96:99] offset:0
	ds_write_b128 v74, v[100:103] offset:32
	ds_write_b128 v74, v[104:107] offset:64
	ds_write_b128 v74, v[108:111] offset:96
	ds_write_b128 v74, v[112:115] offset:128
	ds_write_b128 v74, v[116:119] offset:160
	ds_write_b128 v74, v[120:123] offset:192
	ds_write_b128 v74, v[124:127] offset:224
	s_waitcnt lgkmcnt(0)
	ds_read_b128 v[96:99], v75 offset:0
	ds_read_b128 v[100:103], v75 offset:64
	ds_read_b128 v[104:107], v75 offset:128
	ds_read_b128 v[108:111], v75 offset:192
	ds_read_b128 v[112:115], v75 offset:4096
	ds_read_b128 v[116:119], v75 offset:4160
	ds_read_b128 v[120:123], v75 offset:4224
	ds_read_b128 v[124:127], v75 offset:4288
	s_waitcnt lgkmcnt(0)
	v_mov_b32_e32 v194, 0
	v_mov_b32_e32 v195, 0
.LBB0_734:
	s_waitcnt lgkmcnt(0)
	s_barrier
	ds_read_b128 v[160:163], v201 offset:0
	ds_read_b128 v[164:167], v202 offset:0
	ds_read_b128 v[168:171], v203 offset:0
	ds_read_b128 v[172:175], v204 offset:0
	ds_read_b128 v[176:179], v201 offset:4096
	ds_read_b128 v[180:183], v202 offset:4096
	ds_read_b128 v[230:233], v203 offset:4096
	s_waitcnt lgkmcnt(6)
	v_mfma_f32_16x16x32_bf16 v[64:67], v[160:163], v[96:99], 0
	v_mfma_f32_16x16x32_bf16 v[68:71], v[160:163], v[112:115], 0
	ds_read_b128 v[234:237], v204 offset:4096
	s_add_u32 s16, s22, s10
	s_addc_u32 s17, s23, s11
	s_add_u32 s15, s22, s12
	s_addc_u32 s14, s23, s13
	s_add_u32 s8, s16, 0x3bc00200
	s_addc_u32 s9, s17, 0
	s_add_u32 s6, s15, 0x23a40000
	s_addc_u32 s7, s14, 0
	s_waitcnt lgkmcnt(6)
	v_mfma_f32_16x16x32_bf16 v[64:67], v[164:167], v[100:103], v[64:67]
	v_mfma_f32_16x16x32_bf16 v[68:71], v[164:167], v[116:119], v[68:71]
	ds_read_b128 v[160:163], v201 offset:8192
	s_waitcnt vmcnt(4)
	ds_write_b128 v225, v[136:139] offset:32768
	s_waitcnt lgkmcnt(7)
	v_mfma_f32_16x16x32_bf16 v[64:67], v[168:171], v[104:107], v[64:67]
	v_mfma_f32_16x16x32_bf16 v[68:71], v[168:171], v[120:123], v[68:71]
	ds_read_b128 v[164:167], v202 offset:8192
	ds_write_b128 v226, v[140:143] offset:32768
	s_waitcnt lgkmcnt(8)
	v_mfma_f32_16x16x32_bf16 v[64:67], v[172:175], v[108:111], v[64:67]
	v_mfma_f32_16x16x32_bf16 v[68:71], v[172:175], v[124:127], v[68:71]
	ds_read_b128 v[168:171], v203 offset:8192
	ds_write_b64 v227, v[132:133] offset:32768
	s_waitcnt lgkmcnt(9)
	v_mfma_f32_16x16x32_bf16 v[72:75], v[176:179], v[96:99], 0
	v_mfma_f32_16x16x32_bf16 v[76:79], v[176:179], v[112:115], 0
	ds_read_b128 v[172:175], v204 offset:8192
	ds_write_b64 v228, v[134:135] offset:32768
	s_waitcnt lgkmcnt(10)
	v_mfma_f32_16x16x32_bf16 v[72:75], v[180:183], v[100:103], v[72:75]
	v_mfma_f32_16x16x32_bf16 v[76:79], v[180:183], v[116:119], v[76:79]
	ds_read_b128 v[176:179], v201 offset:12288
	ds_write_b64 v229, v[128:129] offset:32768
	s_waitcnt lgkmcnt(11)
	v_mfma_f32_16x16x32_bf16 v[72:75], v[230:233], v[104:107], v[72:75]
	v_mfma_f32_16x16x32_bf16 v[76:79], v[230:233], v[120:123], v[76:79]
	ds_read_b128 v[180:183], v202 offset:12288
	ds_write_b64 v184, v[130:131] offset:32768
	s_waitcnt lgkmcnt(12)
	v_mfma_f32_16x16x32_bf16 v[72:75], v[234:237], v[108:111], v[72:75]
	v_mfma_f32_16x16x32_bf16 v[76:79], v[234:237], v[124:127], v[76:79]
	ds_read_b128 v[230:233], v203 offset:12288
	global_load_dwordx4 v[132:135], v198, s[8:9]
	s_waitcnt lgkmcnt(12)
	v_mfma_f32_16x16x32_bf16 v[80:83], v[160:163], v[96:99], 0
	v_exp_f32_e32 v64, v64
	v_exp_f32_e32 v65, v65
	v_exp_f32_e32 v66, v66
	v_mfma_f32_16x16x32_bf16 v[84:87], v[160:163], v[112:115], 0
	v_exp_f32_e32 v67, v67
	v_exp_f32_e32 v68, v68
	v_exp_f32_e32 v69, v69
	ds_read_b128 v[234:237], v204 offset:12288
	global_load_dwordx4 v[128:131], v199, s[8:9]
	s_waitcnt lgkmcnt(11)
	v_mfma_f32_16x16x32_bf16 v[80:83], v[164:167], v[100:103], v[80:83]
	v_exp_f32_e32 v70, v70
	v_exp_f32_e32 v71, v71
	v_add_f32_e32 v194, v194, v64
	v_mfma_f32_16x16x32_bf16 v[84:87], v[164:167], v[116:119], v[84:87]
	v_add_f32_e32 v194, v194, v65
	v_add_f32_e32 v194, v194, v66
	v_add_f32_e32 v194, v194, v67
	ds_read_b128 v[160:163], v209 offset:0
	global_load_dwordx4 v[136:139], v196, s[6:7]
	s_waitcnt lgkmcnt(10)
	v_mfma_f32_16x16x32_bf16 v[80:83], v[168:171], v[104:107], v[80:83]
	v_add_f32_e32 v195, v195, v68
	v_add_f32_e32 v195, v195, v69
	v_add_f32_e32 v195, v195, v70
	v_mfma_f32_16x16x32_bf16 v[84:87], v[168:171], v[120:123], v[84:87]
	v_add_f32_e32 v195, v195, v71
	v_cvt_pk_bf16_f32 v64, v64, v65
	v_cvt_pk_bf16_f32 v65, v66, v67
	ds_read_b128 v[164:167], v209 offset:2048
	global_load_dwordx4 v[140:143], v197, s[6:7]
	s_waitcnt lgkmcnt(9)
	v_mfma_f32_16x16x32_bf16 v[80:83], v[172:175], v[108:111], v[80:83]
	v_cvt_pk_bf16_f32 v68, v68, v69
	v_cvt_pk_bf16_f32 v69, v70, v71
	v_mfma_f32_16x16x32_bf16 v[84:87], v[172:175], v[124:127], v[84:87]
	ds_read_b128 v[168:171], v209 offset:4096
	s_waitcnt lgkmcnt(8)
	v_mfma_f32_16x16x32_bf16 v[88:91], v[176:179], v[96:99], 0
	v_exp_f32_e32 v72, v72
	v_exp_f32_e32 v73, v73
	v_exp_f32_e32 v74, v74
	v_mfma_f32_16x16x32_bf16 v[92:95], v[176:179], v[112:115], 0
	v_exp_f32_e32 v75, v75
	v_exp_f32_e32 v76, v76
	v_exp_f32_e32 v77, v77
	ds_read_b128 v[172:175], v209 offset:6144
	s_waitcnt lgkmcnt(7)
	v_mfma_f32_16x16x32_bf16 v[88:91], v[180:183], v[100:103], v[88:91]
	v_exp_f32_e32 v78, v78
	v_exp_f32_e32 v79, v79
	v_add_f32_e32 v194, v194, v72
	v_mfma_f32_16x16x32_bf16 v[92:95], v[180:183], v[116:119], v[92:95]
	v_add_f32_e32 v194, v194, v73
	v_add_f32_e32 v194, v194, v74
	v_add_f32_e32 v194, v194, v75
	ds_read_b128 v[176:179], v209 offset:8192
	s_waitcnt lgkmcnt(6)
	v_mfma_f32_16x16x32_bf16 v[88:91], v[230:233], v[104:107], v[88:91]
	v_add_f32_e32 v195, v195, v76
	v_add_f32_e32 v195, v195, v77
	v_add_f32_e32 v195, v195, v78
	v_mfma_f32_16x16x32_bf16 v[92:95], v[230:233], v[120:123], v[92:95]
	v_add_f32_e32 v195, v195, v79
	v_cvt_pk_bf16_f32 v66, v72, v73
	v_cvt_pk_bf16_f32 v67, v74, v75
	ds_read_b128 v[180:183], v209 offset:10240
	s_waitcnt lgkmcnt(6)
	v_mfma_f32_16x16x32_bf16 v[88:91], v[234:237], v[108:111], v[88:91]
	v_cvt_pk_bf16_f32 v70, v76, v77
	v_cvt_pk_bf16_f32 v71, v78, v79
	v_mfma_f32_16x16x32_bf16 v[92:95], v[234:237], v[124:127], v[92:95]
	ds_read_b128 v[230:233], v209 offset:12288
	s_waitcnt lgkmcnt(6)
	v_mfma_f32_16x16x32_bf16 v[0:3], v[160:163], v[64:67], v[0:3]
	v_exp_f32_e32 v80, v80
	v_exp_f32_e32 v81, v81
	v_exp_f32_e32 v82, v82
	v_mfma_f32_16x16x32_bf16 v[4:7], v[160:163], v[68:71], v[4:7]
	v_exp_f32_e32 v83, v83
	v_exp_f32_e32 v84, v84
	v_exp_f32_e32 v85, v85
	ds_read_b128 v[234:237], v209 offset:14336
	s_waitcnt lgkmcnt(6)
	v_mfma_f32_16x16x32_bf16 v[8:11], v[164:167], v[64:67], v[8:11]
	v_exp_f32_e32 v86, v86
	v_exp_f32_e32 v87, v87
	v_add_f32_e32 v194, v194, v80
	v_mfma_f32_16x16x32_bf16 v[12:15], v[164:167], v[68:71], v[12:15]
	v_add_f32_e32 v194, v194, v81
	v_add_f32_e32 v194, v194, v82
	v_add_f32_e32 v194, v194, v83
	ds_read_b128 v[160:163], v210 offset:0
	s_waitcnt lgkmcnt(6)
	v_mfma_f32_16x16x32_bf16 v[16:19], v[168:171], v[64:67], v[16:19]
	v_add_f32_e32 v195, v195, v84
	v_add_f32_e32 v195, v195, v85
	v_add_f32_e32 v195, v195, v86
	v_mfma_f32_16x16x32_bf16 v[20:23], v[168:171], v[68:71], v[20:23]
	v_add_f32_e32 v195, v195, v87
	v_cvt_pk_bf16_f32 v80, v80, v81
	v_cvt_pk_bf16_f32 v81, v82, v83
	ds_read_b128 v[164:167], v210 offset:2048
	s_waitcnt lgkmcnt(6)
	v_mfma_f32_16x16x32_bf16 v[24:27], v[172:175], v[64:67], v[24:27]
	v_cvt_pk_bf16_f32 v84, v84, v85
	v_cvt_pk_bf16_f32 v85, v86, v87
	v_mfma_f32_16x16x32_bf16 v[28:31], v[172:175], v[68:71], v[28:31]
	ds_read_b128 v[168:171], v210 offset:4096
	s_waitcnt lgkmcnt(6)
	v_mfma_f32_16x16x32_bf16 v[32:35], v[176:179], v[64:67], v[32:35]
	v_exp_f32_e32 v88, v88
	v_exp_f32_e32 v89, v89
	v_exp_f32_e32 v90, v90
	v_mfma_f32_16x16x32_bf16 v[36:39], v[176:179], v[68:71], v[36:39]
	v_exp_f32_e32 v91, v91
	v_exp_f32_e32 v92, v92
	v_exp_f32_e32 v93, v93
	ds_read_b128 v[172:175], v210 offset:6144
	s_waitcnt lgkmcnt(6)
	v_mfma_f32_16x16x32_bf16 v[40:43], v[180:183], v[64:67], v[40:43]
	v_exp_f32_e32 v94, v94
	v_exp_f32_e32 v95, v95
	v_add_f32_e32 v194, v194, v88
	v_mfma_f32_16x16x32_bf16 v[44:47], v[180:183], v[68:71], v[44:47]
	v_add_f32_e32 v194, v194, v89
	v_add_f32_e32 v194, v194, v90
	v_add_f32_e32 v194, v194, v91
	ds_read_b128 v[176:179], v210 offset:8192
	s_waitcnt lgkmcnt(6)
	v_mfma_f32_16x16x32_bf16 v[48:51], v[230:233], v[64:67], v[48:51]
	v_add_f32_e32 v195, v195, v92
	v_add_f32_e32 v195, v195, v93
	v_add_f32_e32 v195, v195, v94
	v_mfma_f32_16x16x32_bf16 v[52:55], v[230:233], v[68:71], v[52:55]
	v_add_f32_e32 v195, v195, v95
	v_cvt_pk_bf16_f32 v82, v88, v89
	v_cvt_pk_bf16_f32 v83, v90, v91
	ds_read_b128 v[180:183], v210 offset:10240
	s_waitcnt lgkmcnt(6)
	v_mfma_f32_16x16x32_bf16 v[56:59], v[234:237], v[64:67], v[56:59]
	v_cvt_pk_bf16_f32 v86, v92, v93
	v_cvt_pk_bf16_f32 v87, v94, v95
	v_mfma_f32_16x16x32_bf16 v[60:63], v[234:237], v[68:71], v[60:63]
	ds_read_b128 v[230:233], v210 offset:12288
	s_waitcnt lgkmcnt(6)
	v_mfma_f32_16x16x32_bf16 v[0:3], v[160:163], v[80:83], v[0:3]
	v_mfma_f32_16x16x32_bf16 v[4:7], v[160:163], v[84:87], v[4:7]
	ds_read_b128 v[234:237], v210 offset:14336
	s_waitcnt lgkmcnt(6)
	v_mfma_f32_16x16x32_bf16 v[8:11], v[164:167], v[80:83], v[8:11]
	v_mfma_f32_16x16x32_bf16 v[12:15], v[164:167], v[84:87], v[12:15]
	ds_read_b128 v[160:163], v201 offset:16384
	s_waitcnt lgkmcnt(6)
	v_mfma_f32_16x16x32_bf16 v[16:19], v[168:171], v[80:83], v[16:19]
	v_mfma_f32_16x16x32_bf16 v[20:23], v[168:171], v[84:87], v[20:23]
	ds_read_b128 v[164:167], v202 offset:16384
	s_waitcnt lgkmcnt(6)
	v_mfma_f32_16x16x32_bf16 v[24:27], v[172:175], v[80:83], v[24:27]
	v_mfma_f32_16x16x32_bf16 v[28:31], v[172:175], v[84:87], v[28:31]
	ds_read_b128 v[168:171], v203 offset:16384
	s_waitcnt lgkmcnt(6)
	v_mfma_f32_16x16x32_bf16 v[32:35], v[176:179], v[80:83], v[32:35]
	v_mfma_f32_16x16x32_bf16 v[36:39], v[176:179], v[84:87], v[36:39]
	ds_read_b128 v[172:175], v204 offset:16384
	s_waitcnt lgkmcnt(6)
	v_mfma_f32_16x16x32_bf16 v[40:43], v[180:183], v[80:83], v[40:43]
	v_mfma_f32_16x16x32_bf16 v[44:47], v[180:183], v[84:87], v[44:47]
	ds_read_b128 v[176:179], v201 offset:20480
	s_waitcnt lgkmcnt(6)
	v_mfma_f32_16x16x32_bf16 v[48:51], v[230:233], v[80:83], v[48:51]
	v_mfma_f32_16x16x32_bf16 v[52:55], v[230:233], v[84:87], v[52:55]
	ds_read_b128 v[180:183], v202 offset:20480
	s_waitcnt lgkmcnt(6)
	v_mfma_f32_16x16x32_bf16 v[56:59], v[234:237], v[80:83], v[56:59]
	v_mfma_f32_16x16x32_bf16 v[60:63], v[234:237], v[84:87], v[60:63]
	ds_read_b128 v[230:233], v203 offset:20480
	s_waitcnt lgkmcnt(6)
	v_mfma_f32_16x16x32_bf16 v[64:67], v[160:163], v[96:99], 0
	v_mfma_f32_16x16x32_bf16 v[68:71], v[160:163], v[112:115], 0
	ds_read_b128 v[234:237], v204 offset:20480
	s_add_u32 s8, s16, 0x3bc00280
	s_addc_u32 s9, s17, 0
	s_add_u32 s6, s15, 0x23a50000
	s_addc_u32 s7, s14, 0
	s_waitcnt lgkmcnt(6)
	v_mfma_f32_16x16x32_bf16 v[64:67], v[164:167], v[100:103], v[64:67]
	v_mfma_f32_16x16x32_bf16 v[68:71], v[164:167], v[116:119], v[68:71]
	ds_read_b128 v[160:163], v201 offset:24576
	s_waitcnt vmcnt(4)
	ds_write_b128 v225, v[152:155] offset:49152
	s_waitcnt lgkmcnt(7)
	v_mfma_f32_16x16x32_bf16 v[64:67], v[168:171], v[104:107], v[64:67]
	v_mfma_f32_16x16x32_bf16 v[68:71], v[168:171], v[120:123], v[68:71]
	ds_read_b128 v[164:167], v202 offset:24576
	ds_write_b128 v226, v[156:159] offset:49152
	s_waitcnt lgkmcnt(8)
	v_mfma_f32_16x16x32_bf16 v[64:67], v[172:175], v[108:111], v[64:67]
	v_mfma_f32_16x16x32_bf16 v[68:71], v[172:175], v[124:127], v[68:71]
	ds_read_b128 v[168:171], v203 offset:24576
	ds_write_b64 v227, v[148:149] offset:49152
	s_waitcnt lgkmcnt(9)
	v_mfma_f32_16x16x32_bf16 v[72:75], v[176:179], v[96:99], 0
	v_mfma_f32_16x16x32_bf16 v[76:79], v[176:179], v[112:115], 0
	ds_read_b128 v[172:175], v204 offset:24576
	ds_write_b64 v228, v[150:151] offset:49152
	s_waitcnt lgkmcnt(10)
	v_mfma_f32_16x16x32_bf16 v[72:75], v[180:183], v[100:103], v[72:75]
	v_mfma_f32_16x16x32_bf16 v[76:79], v[180:183], v[116:119], v[76:79]
	ds_read_b128 v[176:179], v201 offset:28672
	ds_write_b64 v229, v[144:145] offset:49152
	s_waitcnt lgkmcnt(11)
	v_mfma_f32_16x16x32_bf16 v[72:75], v[230:233], v[104:107], v[72:75]
	v_mfma_f32_16x16x32_bf16 v[76:79], v[230:233], v[120:123], v[76:79]
	ds_read_b128 v[180:183], v202 offset:28672
	ds_write_b64 v184, v[146:147] offset:49152
	s_waitcnt lgkmcnt(12)
	v_mfma_f32_16x16x32_bf16 v[72:75], v[234:237], v[108:111], v[72:75]
	v_mfma_f32_16x16x32_bf16 v[76:79], v[234:237], v[124:127], v[76:79]
	ds_read_b128 v[230:233], v203 offset:28672
	global_load_dwordx4 v[148:151], v198, s[8:9]
	s_waitcnt lgkmcnt(12)
	v_mfma_f32_16x16x32_bf16 v[80:83], v[160:163], v[96:99], 0
	v_exp_f32_e32 v64, v64
	v_exp_f32_e32 v65, v65
	v_exp_f32_e32 v66, v66
	v_mfma_f32_16x16x32_bf16 v[84:87], v[160:163], v[112:115], 0
	v_exp_f32_e32 v67, v67
	v_exp_f32_e32 v68, v68
	v_exp_f32_e32 v69, v69
	ds_read_b128 v[234:237], v204 offset:28672
	global_load_dwordx4 v[144:147], v199, s[8:9]
	s_waitcnt lgkmcnt(11)
	v_mfma_f32_16x16x32_bf16 v[80:83], v[164:167], v[100:103], v[80:83]
	v_exp_f32_e32 v70, v70
	v_exp_f32_e32 v71, v71
	v_add_f32_e32 v194, v194, v64
	v_mfma_f32_16x16x32_bf16 v[84:87], v[164:167], v[116:119], v[84:87]
	v_add_f32_e32 v194, v194, v65
	v_add_f32_e32 v194, v194, v66
	v_add_f32_e32 v194, v194, v67
	ds_read_b128 v[160:163], v209 offset:16384
	global_load_dwordx4 v[152:155], v196, s[6:7]
	s_waitcnt lgkmcnt(10)
	v_mfma_f32_16x16x32_bf16 v[80:83], v[168:171], v[104:107], v[80:83]
	v_add_f32_e32 v195, v195, v68
	v_add_f32_e32 v195, v195, v69
	v_add_f32_e32 v195, v195, v70
	v_mfma_f32_16x16x32_bf16 v[84:87], v[168:171], v[120:123], v[84:87]
	v_add_f32_e32 v195, v195, v71
	v_cvt_pk_bf16_f32 v64, v64, v65
	v_cvt_pk_bf16_f32 v65, v66, v67
	ds_read_b128 v[164:167], v209 offset:18432
	global_load_dwordx4 v[156:159], v197, s[6:7]
	s_waitcnt lgkmcnt(9)
	v_mfma_f32_16x16x32_bf16 v[80:83], v[172:175], v[108:111], v[80:83]
	v_cvt_pk_bf16_f32 v68, v68, v69
	v_cvt_pk_bf16_f32 v69, v70, v71
	v_mfma_f32_16x16x32_bf16 v[84:87], v[172:175], v[124:127], v[84:87]
	ds_read_b128 v[168:171], v209 offset:20480
	s_waitcnt lgkmcnt(8)
	v_mfma_f32_16x16x32_bf16 v[88:91], v[176:179], v[96:99], 0
	v_exp_f32_e32 v72, v72
	v_exp_f32_e32 v73, v73
	v_exp_f32_e32 v74, v74
	v_mfma_f32_16x16x32_bf16 v[92:95], v[176:179], v[112:115], 0
	v_exp_f32_e32 v75, v75
	v_exp_f32_e32 v76, v76
	v_exp_f32_e32 v77, v77
	ds_read_b128 v[172:175], v209 offset:22528
	s_waitcnt lgkmcnt(7)
	v_mfma_f32_16x16x32_bf16 v[88:91], v[180:183], v[100:103], v[88:91]
	v_exp_f32_e32 v78, v78
	v_exp_f32_e32 v79, v79
	v_add_f32_e32 v194, v194, v72
	v_mfma_f32_16x16x32_bf16 v[92:95], v[180:183], v[116:119], v[92:95]
	v_add_f32_e32 v194, v194, v73
	v_add_f32_e32 v194, v194, v74
	v_add_f32_e32 v194, v194, v75
	ds_read_b128 v[176:179], v209 offset:24576
	s_waitcnt lgkmcnt(6)
	v_mfma_f32_16x16x32_bf16 v[88:91], v[230:233], v[104:107], v[88:91]
	v_add_f32_e32 v195, v195, v76
	v_add_f32_e32 v195, v195, v77
	v_add_f32_e32 v195, v195, v78
	v_mfma_f32_16x16x32_bf16 v[92:95], v[230:233], v[120:123], v[92:95]
	v_add_f32_e32 v195, v195, v79
	v_cvt_pk_bf16_f32 v66, v72, v73
	v_cvt_pk_bf16_f32 v67, v74, v75
	ds_read_b128 v[180:183], v209 offset:26624
	s_waitcnt lgkmcnt(6)
	v_mfma_f32_16x16x32_bf16 v[88:91], v[234:237], v[108:111], v[88:91]
	v_cvt_pk_bf16_f32 v70, v76, v77
	v_cvt_pk_bf16_f32 v71, v78, v79
	v_mfma_f32_16x16x32_bf16 v[92:95], v[234:237], v[124:127], v[92:95]
	ds_read_b128 v[230:233], v209 offset:28672
	s_waitcnt lgkmcnt(6)
	v_mfma_f32_16x16x32_bf16 v[0:3], v[160:163], v[64:67], v[0:3]
	v_exp_f32_e32 v80, v80
	v_exp_f32_e32 v81, v81
	v_exp_f32_e32 v82, v82
	v_mfma_f32_16x16x32_bf16 v[4:7], v[160:163], v[68:71], v[4:7]
	v_exp_f32_e32 v83, v83
	v_exp_f32_e32 v84, v84
	v_exp_f32_e32 v85, v85
	ds_read_b128 v[234:237], v209 offset:30720
	s_waitcnt lgkmcnt(6)
	v_mfma_f32_16x16x32_bf16 v[8:11], v[164:167], v[64:67], v[8:11]
	v_exp_f32_e32 v86, v86
	v_exp_f32_e32 v87, v87
	v_add_f32_e32 v194, v194, v80
	v_mfma_f32_16x16x32_bf16 v[12:15], v[164:167], v[68:71], v[12:15]
	v_add_f32_e32 v194, v194, v81
	v_add_f32_e32 v194, v194, v82
	v_add_f32_e32 v194, v194, v83
	ds_read_b128 v[160:163], v210 offset:16384
	s_waitcnt lgkmcnt(6)
	v_mfma_f32_16x16x32_bf16 v[16:19], v[168:171], v[64:67], v[16:19]
	v_add_f32_e32 v195, v195, v84
	v_add_f32_e32 v195, v195, v85
	v_add_f32_e32 v195, v195, v86
	v_mfma_f32_16x16x32_bf16 v[20:23], v[168:171], v[68:71], v[20:23]
	v_add_f32_e32 v195, v195, v87
	v_cvt_pk_bf16_f32 v80, v80, v81
	v_cvt_pk_bf16_f32 v81, v82, v83
	ds_read_b128 v[164:167], v210 offset:18432
	s_waitcnt lgkmcnt(6)
	v_mfma_f32_16x16x32_bf16 v[24:27], v[172:175], v[64:67], v[24:27]
	v_cvt_pk_bf16_f32 v84, v84, v85
	v_cvt_pk_bf16_f32 v85, v86, v87
	v_mfma_f32_16x16x32_bf16 v[28:31], v[172:175], v[68:71], v[28:31]
	ds_read_b128 v[168:171], v210 offset:20480
	s_waitcnt lgkmcnt(6)
	v_mfma_f32_16x16x32_bf16 v[32:35], v[176:179], v[64:67], v[32:35]
	v_exp_f32_e32 v88, v88
	v_exp_f32_e32 v89, v89
	v_exp_f32_e32 v90, v90
	v_mfma_f32_16x16x32_bf16 v[36:39], v[176:179], v[68:71], v[36:39]
	v_exp_f32_e32 v91, v91
	v_exp_f32_e32 v92, v92
	v_exp_f32_e32 v93, v93
	ds_read_b128 v[172:175], v210 offset:22528
	s_waitcnt lgkmcnt(6)
	v_mfma_f32_16x16x32_bf16 v[40:43], v[180:183], v[64:67], v[40:43]
	v_exp_f32_e32 v94, v94
	v_exp_f32_e32 v95, v95
	v_add_f32_e32 v194, v194, v88
	v_mfma_f32_16x16x32_bf16 v[44:47], v[180:183], v[68:71], v[44:47]
	v_add_f32_e32 v194, v194, v89
	v_add_f32_e32 v194, v194, v90
	v_add_f32_e32 v194, v194, v91
	ds_read_b128 v[176:179], v210 offset:24576
	s_waitcnt lgkmcnt(6)
	v_mfma_f32_16x16x32_bf16 v[48:51], v[230:233], v[64:67], v[48:51]
	v_add_f32_e32 v195, v195, v92
	v_add_f32_e32 v195, v195, v93
	v_add_f32_e32 v195, v195, v94
	v_mfma_f32_16x16x32_bf16 v[52:55], v[230:233], v[68:71], v[52:55]
	v_add_f32_e32 v195, v195, v95
	v_cvt_pk_bf16_f32 v82, v88, v89
	v_cvt_pk_bf16_f32 v83, v90, v91
	ds_read_b128 v[180:183], v210 offset:26624
	s_waitcnt lgkmcnt(6)
	v_mfma_f32_16x16x32_bf16 v[56:59], v[234:237], v[64:67], v[56:59]
	v_cvt_pk_bf16_f32 v86, v92, v93
	v_cvt_pk_bf16_f32 v87, v94, v95
	v_mfma_f32_16x16x32_bf16 v[60:63], v[234:237], v[68:71], v[60:63]
	ds_read_b128 v[230:233], v210 offset:28672
	s_waitcnt lgkmcnt(6)
	v_mfma_f32_16x16x32_bf16 v[0:3], v[160:163], v[80:83], v[0:3]
	v_mfma_f32_16x16x32_bf16 v[4:7], v[160:163], v[84:87], v[4:7]
	ds_read_b128 v[234:237], v210 offset:30720
	s_waitcnt lgkmcnt(6)
	v_mfma_f32_16x16x32_bf16 v[8:11], v[164:167], v[80:83], v[8:11]
	v_mfma_f32_16x16x32_bf16 v[12:15], v[164:167], v[84:87], v[12:15]
	s_waitcnt lgkmcnt(5)
	v_mfma_f32_16x16x32_bf16 v[16:19], v[168:171], v[80:83], v[16:19]
	v_mfma_f32_16x16x32_bf16 v[20:23], v[168:171], v[84:87], v[20:23]
	s_waitcnt lgkmcnt(4)
	v_mfma_f32_16x16x32_bf16 v[24:27], v[172:175], v[80:83], v[24:27]
	v_mfma_f32_16x16x32_bf16 v[28:31], v[172:175], v[84:87], v[28:31]
	s_waitcnt lgkmcnt(3)
	v_mfma_f32_16x16x32_bf16 v[32:35], v[176:179], v[80:83], v[32:35]
	v_mfma_f32_16x16x32_bf16 v[36:39], v[176:179], v[84:87], v[36:39]
	s_waitcnt lgkmcnt(2)
	v_mfma_f32_16x16x32_bf16 v[40:43], v[180:183], v[80:83], v[40:43]
	v_mfma_f32_16x16x32_bf16 v[44:47], v[180:183], v[84:87], v[44:47]
	s_waitcnt lgkmcnt(1)
	v_mfma_f32_16x16x32_bf16 v[48:51], v[230:233], v[80:83], v[48:51]
	v_mfma_f32_16x16x32_bf16 v[52:55], v[230:233], v[84:87], v[52:55]
	s_waitcnt lgkmcnt(0)
	v_mfma_f32_16x16x32_bf16 v[56:59], v[234:237], v[80:83], v[56:59]
	v_mfma_f32_16x16x32_bf16 v[60:63], v[234:237], v[84:87], v[60:63]
	s_waitcnt lgkmcnt(0)
	s_barrier
	ds_read_b128 v[160:163], v201 offset:32768
	ds_read_b128 v[164:167], v202 offset:32768
	ds_read_b128 v[168:171], v203 offset:32768
	ds_read_b128 v[172:175], v204 offset:32768
	ds_read_b128 v[176:179], v201 offset:36864
	ds_read_b128 v[180:183], v202 offset:36864
	ds_read_b128 v[230:233], v203 offset:36864
	s_waitcnt lgkmcnt(6)
	v_mfma_f32_16x16x32_bf16 v[64:67], v[160:163], v[96:99], 0
	v_mfma_f32_16x16x32_bf16 v[68:71], v[160:163], v[112:115], 0
	ds_read_b128 v[234:237], v204 offset:36864
	s_add_u32 s8, s16, 0x3bc00300
	s_addc_u32 s9, s17, 0
	s_add_u32 s6, s15, 0x23a60000
	s_addc_u32 s7, s14, 0
	s_waitcnt lgkmcnt(6)
	v_mfma_f32_16x16x32_bf16 v[64:67], v[164:167], v[100:103], v[64:67]
	v_mfma_f32_16x16x32_bf16 v[68:71], v[164:167], v[116:119], v[68:71]
	ds_read_b128 v[160:163], v201 offset:40960
	s_waitcnt vmcnt(4)
	ds_write_b128 v225, v[136:139] offset:0
	s_waitcnt lgkmcnt(7)
	v_mfma_f32_16x16x32_bf16 v[64:67], v[168:171], v[104:107], v[64:67]
	v_mfma_f32_16x16x32_bf16 v[68:71], v[168:171], v[120:123], v[68:71]
	ds_read_b128 v[164:167], v202 offset:40960
	ds_write_b128 v226, v[140:143] offset:0
	s_waitcnt lgkmcnt(8)
	v_mfma_f32_16x16x32_bf16 v[64:67], v[172:175], v[108:111], v[64:67]
	v_mfma_f32_16x16x32_bf16 v[68:71], v[172:175], v[124:127], v[68:71]
	ds_read_b128 v[168:171], v203 offset:40960
	ds_write_b64 v227, v[132:133] offset:0
	s_waitcnt lgkmcnt(9)
	v_mfma_f32_16x16x32_bf16 v[72:75], v[176:179], v[96:99], 0
	v_mfma_f32_16x16x32_bf16 v[76:79], v[176:179], v[112:115], 0
	ds_read_b128 v[172:175], v204 offset:40960
	ds_write_b64 v228, v[134:135] offset:0
	s_waitcnt lgkmcnt(10)
	v_mfma_f32_16x16x32_bf16 v[72:75], v[180:183], v[100:103], v[72:75]
	v_mfma_f32_16x16x32_bf16 v[76:79], v[180:183], v[116:119], v[76:79]
	ds_read_b128 v[176:179], v201 offset:45056
	ds_write_b64 v229, v[128:129] offset:0
	s_waitcnt lgkmcnt(11)
	v_mfma_f32_16x16x32_bf16 v[72:75], v[230:233], v[104:107], v[72:75]
	v_mfma_f32_16x16x32_bf16 v[76:79], v[230:233], v[120:123], v[76:79]
	ds_read_b128 v[180:183], v202 offset:45056
	ds_write_b64 v184, v[130:131] offset:0
	s_waitcnt lgkmcnt(12)
	v_mfma_f32_16x16x32_bf16 v[72:75], v[234:237], v[108:111], v[72:75]
	v_mfma_f32_16x16x32_bf16 v[76:79], v[234:237], v[124:127], v[76:79]
	ds_read_b128 v[230:233], v203 offset:45056
	global_load_dwordx4 v[132:135], v198, s[8:9]
	s_waitcnt lgkmcnt(12)
	v_mfma_f32_16x16x32_bf16 v[80:83], v[160:163], v[96:99], 0
	v_exp_f32_e32 v64, v64
	v_exp_f32_e32 v65, v65
	v_exp_f32_e32 v66, v66
	v_mfma_f32_16x16x32_bf16 v[84:87], v[160:163], v[112:115], 0
	v_exp_f32_e32 v67, v67
	v_exp_f32_e32 v68, v68
	v_exp_f32_e32 v69, v69
	ds_read_b128 v[234:237], v204 offset:45056
	global_load_dwordx4 v[128:131], v199, s[8:9]
	s_waitcnt lgkmcnt(11)
	v_mfma_f32_16x16x32_bf16 v[80:83], v[164:167], v[100:103], v[80:83]
	v_exp_f32_e32 v70, v70
	v_exp_f32_e32 v71, v71
	v_add_f32_e32 v194, v194, v64
	v_mfma_f32_16x16x32_bf16 v[84:87], v[164:167], v[116:119], v[84:87]
	v_add_f32_e32 v194, v194, v65
	v_add_f32_e32 v194, v194, v66
	v_add_f32_e32 v194, v194, v67
	ds_read_b128 v[160:163], v209 offset:32768
	global_load_dwordx4 v[136:139], v196, s[6:7]
	s_waitcnt lgkmcnt(10)
	v_mfma_f32_16x16x32_bf16 v[80:83], v[168:171], v[104:107], v[80:83]
	v_add_f32_e32 v195, v195, v68
	v_add_f32_e32 v195, v195, v69
	v_add_f32_e32 v195, v195, v70
	v_mfma_f32_16x16x32_bf16 v[84:87], v[168:171], v[120:123], v[84:87]
	v_add_f32_e32 v195, v195, v71
	v_cvt_pk_bf16_f32 v64, v64, v65
	v_cvt_pk_bf16_f32 v65, v66, v67
	ds_read_b128 v[164:167], v209 offset:34816
	global_load_dwordx4 v[140:143], v197, s[6:7]
	s_waitcnt lgkmcnt(9)
	v_mfma_f32_16x16x32_bf16 v[80:83], v[172:175], v[108:111], v[80:83]
	v_cvt_pk_bf16_f32 v68, v68, v69
	v_cvt_pk_bf16_f32 v69, v70, v71
	v_mfma_f32_16x16x32_bf16 v[84:87], v[172:175], v[124:127], v[84:87]
	ds_read_b128 v[168:171], v209 offset:36864
	s_waitcnt lgkmcnt(8)
	v_mfma_f32_16x16x32_bf16 v[88:91], v[176:179], v[96:99], 0
	v_exp_f32_e32 v72, v72
	v_exp_f32_e32 v73, v73
	v_exp_f32_e32 v74, v74
	v_mfma_f32_16x16x32_bf16 v[92:95], v[176:179], v[112:115], 0
	v_exp_f32_e32 v75, v75
	v_exp_f32_e32 v76, v76
	v_exp_f32_e32 v77, v77
	ds_read_b128 v[172:175], v209 offset:38912
	s_waitcnt lgkmcnt(7)
	v_mfma_f32_16x16x32_bf16 v[88:91], v[180:183], v[100:103], v[88:91]
	v_exp_f32_e32 v78, v78
	v_exp_f32_e32 v79, v79
	v_add_f32_e32 v194, v194, v72
	v_mfma_f32_16x16x32_bf16 v[92:95], v[180:183], v[116:119], v[92:95]
	v_add_f32_e32 v194, v194, v73
	v_add_f32_e32 v194, v194, v74
	v_add_f32_e32 v194, v194, v75
	ds_read_b128 v[176:179], v209 offset:40960
	s_waitcnt lgkmcnt(6)
	v_mfma_f32_16x16x32_bf16 v[88:91], v[230:233], v[104:107], v[88:91]
	v_add_f32_e32 v195, v195, v76
	v_add_f32_e32 v195, v195, v77
	v_add_f32_e32 v195, v195, v78
	v_mfma_f32_16x16x32_bf16 v[92:95], v[230:233], v[120:123], v[92:95]
	v_add_f32_e32 v195, v195, v79
	v_cvt_pk_bf16_f32 v66, v72, v73
	v_cvt_pk_bf16_f32 v67, v74, v75
	ds_read_b128 v[180:183], v209 offset:43008
	s_waitcnt lgkmcnt(6)
	v_mfma_f32_16x16x32_bf16 v[88:91], v[234:237], v[108:111], v[88:91]
	v_cvt_pk_bf16_f32 v70, v76, v77
	v_cvt_pk_bf16_f32 v71, v78, v79
	v_mfma_f32_16x16x32_bf16 v[92:95], v[234:237], v[124:127], v[92:95]
	ds_read_b128 v[230:233], v209 offset:45056
	s_waitcnt lgkmcnt(6)
	v_mfma_f32_16x16x32_bf16 v[0:3], v[160:163], v[64:67], v[0:3]
	v_exp_f32_e32 v80, v80
	v_exp_f32_e32 v81, v81
	v_exp_f32_e32 v82, v82
	v_mfma_f32_16x16x32_bf16 v[4:7], v[160:163], v[68:71], v[4:7]
	v_exp_f32_e32 v83, v83
	v_exp_f32_e32 v84, v84
	v_exp_f32_e32 v85, v85
	ds_read_b128 v[234:237], v209 offset:47104
	s_waitcnt lgkmcnt(6)
	v_mfma_f32_16x16x32_bf16 v[8:11], v[164:167], v[64:67], v[8:11]
	v_exp_f32_e32 v86, v86
	v_exp_f32_e32 v87, v87
	v_add_f32_e32 v194, v194, v80
	v_mfma_f32_16x16x32_bf16 v[12:15], v[164:167], v[68:71], v[12:15]
	v_add_f32_e32 v194, v194, v81
	v_add_f32_e32 v194, v194, v82
	v_add_f32_e32 v194, v194, v83
	ds_read_b128 v[160:163], v210 offset:32768
	s_waitcnt lgkmcnt(6)
	v_mfma_f32_16x16x32_bf16 v[16:19], v[168:171], v[64:67], v[16:19]
	v_add_f32_e32 v195, v195, v84
	v_add_f32_e32 v195, v195, v85
	v_add_f32_e32 v195, v195, v86
	v_mfma_f32_16x16x32_bf16 v[20:23], v[168:171], v[68:71], v[20:23]
	v_add_f32_e32 v195, v195, v87
	v_cvt_pk_bf16_f32 v80, v80, v81
	v_cvt_pk_bf16_f32 v81, v82, v83
	ds_read_b128 v[164:167], v210 offset:34816
	s_waitcnt lgkmcnt(6)
	v_mfma_f32_16x16x32_bf16 v[24:27], v[172:175], v[64:67], v[24:27]
	v_cvt_pk_bf16_f32 v84, v84, v85
	v_cvt_pk_bf16_f32 v85, v86, v87
	v_mfma_f32_16x16x32_bf16 v[28:31], v[172:175], v[68:71], v[28:31]
	ds_read_b128 v[168:171], v210 offset:36864
	s_waitcnt lgkmcnt(6)
	v_mfma_f32_16x16x32_bf16 v[32:35], v[176:179], v[64:67], v[32:35]
	v_exp_f32_e32 v88, v88
	v_exp_f32_e32 v89, v89
	v_exp_f32_e32 v90, v90
	v_mfma_f32_16x16x32_bf16 v[36:39], v[176:179], v[68:71], v[36:39]
	v_exp_f32_e32 v91, v91
	v_exp_f32_e32 v92, v92
	v_exp_f32_e32 v93, v93
	ds_read_b128 v[172:175], v210 offset:38912
	s_waitcnt lgkmcnt(6)
	v_mfma_f32_16x16x32_bf16 v[40:43], v[180:183], v[64:67], v[40:43]
	v_exp_f32_e32 v94, v94
	v_exp_f32_e32 v95, v95
	v_add_f32_e32 v194, v194, v88
	v_mfma_f32_16x16x32_bf16 v[44:47], v[180:183], v[68:71], v[44:47]
	v_add_f32_e32 v194, v194, v89
	v_add_f32_e32 v194, v194, v90
	v_add_f32_e32 v194, v194, v91
	ds_read_b128 v[176:179], v210 offset:40960
	s_waitcnt lgkmcnt(6)
	v_mfma_f32_16x16x32_bf16 v[48:51], v[230:233], v[64:67], v[48:51]
	v_add_f32_e32 v195, v195, v92
	v_add_f32_e32 v195, v195, v93
	v_add_f32_e32 v195, v195, v94
	v_mfma_f32_16x16x32_bf16 v[52:55], v[230:233], v[68:71], v[52:55]
	v_add_f32_e32 v195, v195, v95
	v_cvt_pk_bf16_f32 v82, v88, v89
	v_cvt_pk_bf16_f32 v83, v90, v91
	ds_read_b128 v[180:183], v210 offset:43008
	s_waitcnt lgkmcnt(6)
	v_mfma_f32_16x16x32_bf16 v[56:59], v[234:237], v[64:67], v[56:59]
	v_cvt_pk_bf16_f32 v86, v92, v93
	v_cvt_pk_bf16_f32 v87, v94, v95
	v_mfma_f32_16x16x32_bf16 v[60:63], v[234:237], v[68:71], v[60:63]
	ds_read_b128 v[230:233], v210 offset:45056
	s_waitcnt lgkmcnt(6)
	v_mfma_f32_16x16x32_bf16 v[0:3], v[160:163], v[80:83], v[0:3]
	v_mfma_f32_16x16x32_bf16 v[4:7], v[160:163], v[84:87], v[4:7]
	ds_read_b128 v[234:237], v210 offset:47104
	s_waitcnt lgkmcnt(6)
	v_mfma_f32_16x16x32_bf16 v[8:11], v[164:167], v[80:83], v[8:11]
	v_mfma_f32_16x16x32_bf16 v[12:15], v[164:167], v[84:87], v[12:15]
	ds_read_b128 v[160:163], v201 offset:49152
	s_waitcnt lgkmcnt(6)
	v_mfma_f32_16x16x32_bf16 v[16:19], v[168:171], v[80:83], v[16:19]
	v_mfma_f32_16x16x32_bf16 v[20:23], v[168:171], v[84:87], v[20:23]
	ds_read_b128 v[164:167], v202 offset:49152
	s_waitcnt lgkmcnt(6)
	v_mfma_f32_16x16x32_bf16 v[24:27], v[172:175], v[80:83], v[24:27]
	v_mfma_f32_16x16x32_bf16 v[28:31], v[172:175], v[84:87], v[28:31]
	ds_read_b128 v[168:171], v203 offset:49152
	s_waitcnt lgkmcnt(6)
	v_mfma_f32_16x16x32_bf16 v[32:35], v[176:179], v[80:83], v[32:35]
	v_mfma_f32_16x16x32_bf16 v[36:39], v[176:179], v[84:87], v[36:39]
	ds_read_b128 v[172:175], v204 offset:49152
	s_waitcnt lgkmcnt(6)
	v_mfma_f32_16x16x32_bf16 v[40:43], v[180:183], v[80:83], v[40:43]
	v_mfma_f32_16x16x32_bf16 v[44:47], v[180:183], v[84:87], v[44:47]
	ds_read_b128 v[176:179], v201 offset:53248
	s_waitcnt lgkmcnt(6)
	v_mfma_f32_16x16x32_bf16 v[48:51], v[230:233], v[80:83], v[48:51]
	v_mfma_f32_16x16x32_bf16 v[52:55], v[230:233], v[84:87], v[52:55]
	ds_read_b128 v[180:183], v202 offset:53248
	s_waitcnt lgkmcnt(6)
	v_mfma_f32_16x16x32_bf16 v[56:59], v[234:237], v[80:83], v[56:59]
	v_mfma_f32_16x16x32_bf16 v[60:63], v[234:237], v[84:87], v[60:63]
	ds_read_b128 v[230:233], v203 offset:53248
	s_waitcnt lgkmcnt(6)
	v_mfma_f32_16x16x32_bf16 v[64:67], v[160:163], v[96:99], 0
	v_mfma_f32_16x16x32_bf16 v[68:71], v[160:163], v[112:115], 0
	ds_read_b128 v[234:237], v204 offset:53248
	s_add_u32 s8, s16, 0x3bc00380
	s_addc_u32 s9, s17, 0
	s_add_u32 s6, s15, 0x23a70000
	s_addc_u32 s7, s14, 0
	s_waitcnt lgkmcnt(6)
	v_mfma_f32_16x16x32_bf16 v[64:67], v[164:167], v[100:103], v[64:67]
	v_mfma_f32_16x16x32_bf16 v[68:71], v[164:167], v[116:119], v[68:71]
	ds_read_b128 v[160:163], v201 offset:57344
	s_waitcnt vmcnt(4)
	ds_write_b128 v225, v[152:155] offset:16384
	s_waitcnt lgkmcnt(7)
	v_mfma_f32_16x16x32_bf16 v[64:67], v[168:171], v[104:107], v[64:67]
	v_mfma_f32_16x16x32_bf16 v[68:71], v[168:171], v[120:123], v[68:71]
	ds_read_b128 v[164:167], v202 offset:57344
	ds_write_b128 v226, v[156:159] offset:16384
	s_waitcnt lgkmcnt(8)
	v_mfma_f32_16x16x32_bf16 v[64:67], v[172:175], v[108:111], v[64:67]
	v_mfma_f32_16x16x32_bf16 v[68:71], v[172:175], v[124:127], v[68:71]
	ds_read_b128 v[168:171], v203 offset:57344
	ds_write_b64 v227, v[148:149] offset:16384
	s_waitcnt lgkmcnt(9)
	v_mfma_f32_16x16x32_bf16 v[72:75], v[176:179], v[96:99], 0
	v_mfma_f32_16x16x32_bf16 v[76:79], v[176:179], v[112:115], 0
	ds_read_b128 v[172:175], v204 offset:57344
	ds_write_b64 v228, v[150:151] offset:16384
	s_waitcnt lgkmcnt(10)
	v_mfma_f32_16x16x32_bf16 v[72:75], v[180:183], v[100:103], v[72:75]
	v_mfma_f32_16x16x32_bf16 v[76:79], v[180:183], v[116:119], v[76:79]
	ds_read_b128 v[176:179], v201 offset:61440
	ds_write_b64 v229, v[144:145] offset:16384
	s_waitcnt lgkmcnt(11)
	v_mfma_f32_16x16x32_bf16 v[72:75], v[230:233], v[104:107], v[72:75]
	v_mfma_f32_16x16x32_bf16 v[76:79], v[230:233], v[120:123], v[76:79]
	ds_read_b128 v[180:183], v202 offset:61440
	ds_write_b64 v184, v[146:147] offset:16384
	s_waitcnt lgkmcnt(12)
	v_mfma_f32_16x16x32_bf16 v[72:75], v[234:237], v[108:111], v[72:75]
	v_mfma_f32_16x16x32_bf16 v[76:79], v[234:237], v[124:127], v[76:79]
	ds_read_b128 v[230:233], v203 offset:61440
	global_load_dwordx4 v[148:151], v198, s[8:9]
	s_waitcnt lgkmcnt(12)
	v_mfma_f32_16x16x32_bf16 v[80:83], v[160:163], v[96:99], 0
	v_exp_f32_e32 v64, v64
	v_exp_f32_e32 v65, v65
	v_exp_f32_e32 v66, v66
	v_mfma_f32_16x16x32_bf16 v[84:87], v[160:163], v[112:115], 0
	v_exp_f32_e32 v67, v67
	v_exp_f32_e32 v68, v68
	v_exp_f32_e32 v69, v69
	ds_read_b128 v[234:237], v204 offset:61440
	global_load_dwordx4 v[144:147], v199, s[8:9]
	s_waitcnt lgkmcnt(11)
	v_mfma_f32_16x16x32_bf16 v[80:83], v[164:167], v[100:103], v[80:83]
	v_exp_f32_e32 v70, v70
	v_exp_f32_e32 v71, v71
	v_add_f32_e32 v194, v194, v64
	v_mfma_f32_16x16x32_bf16 v[84:87], v[164:167], v[116:119], v[84:87]
	v_add_f32_e32 v194, v194, v65
	v_add_f32_e32 v194, v194, v66
	v_add_f32_e32 v194, v194, v67
	ds_read_b128 v[160:163], v209 offset:49152
	global_load_dwordx4 v[152:155], v196, s[6:7]
	s_waitcnt lgkmcnt(10)
	v_mfma_f32_16x16x32_bf16 v[80:83], v[168:171], v[104:107], v[80:83]
	v_add_f32_e32 v195, v195, v68
	v_add_f32_e32 v195, v195, v69
	v_add_f32_e32 v195, v195, v70
	v_mfma_f32_16x16x32_bf16 v[84:87], v[168:171], v[120:123], v[84:87]
	v_add_f32_e32 v195, v195, v71
	v_cvt_pk_bf16_f32 v64, v64, v65
	v_cvt_pk_bf16_f32 v65, v66, v67
	ds_read_b128 v[164:167], v209 offset:51200
	global_load_dwordx4 v[156:159], v197, s[6:7]
	s_waitcnt lgkmcnt(9)
	v_mfma_f32_16x16x32_bf16 v[80:83], v[172:175], v[108:111], v[80:83]
	v_cvt_pk_bf16_f32 v68, v68, v69
	v_cvt_pk_bf16_f32 v69, v70, v71
	v_mfma_f32_16x16x32_bf16 v[84:87], v[172:175], v[124:127], v[84:87]
	ds_read_b128 v[168:171], v209 offset:53248
	s_waitcnt lgkmcnt(8)
	v_mfma_f32_16x16x32_bf16 v[88:91], v[176:179], v[96:99], 0
	v_exp_f32_e32 v72, v72
	v_exp_f32_e32 v73, v73
	v_exp_f32_e32 v74, v74
	v_mfma_f32_16x16x32_bf16 v[92:95], v[176:179], v[112:115], 0
	v_exp_f32_e32 v75, v75
	v_exp_f32_e32 v76, v76
	v_exp_f32_e32 v77, v77
	ds_read_b128 v[172:175], v209 offset:55296
	s_waitcnt lgkmcnt(7)
	v_mfma_f32_16x16x32_bf16 v[88:91], v[180:183], v[100:103], v[88:91]
	v_exp_f32_e32 v78, v78
	v_exp_f32_e32 v79, v79
	v_add_f32_e32 v194, v194, v72
	v_mfma_f32_16x16x32_bf16 v[92:95], v[180:183], v[116:119], v[92:95]
	v_add_f32_e32 v194, v194, v73
	v_add_f32_e32 v194, v194, v74
	v_add_f32_e32 v194, v194, v75
	ds_read_b128 v[176:179], v209 offset:57344
	s_waitcnt lgkmcnt(6)
	v_mfma_f32_16x16x32_bf16 v[88:91], v[230:233], v[104:107], v[88:91]
	v_add_f32_e32 v195, v195, v76
	v_add_f32_e32 v195, v195, v77
	v_add_f32_e32 v195, v195, v78
	v_mfma_f32_16x16x32_bf16 v[92:95], v[230:233], v[120:123], v[92:95]
	v_add_f32_e32 v195, v195, v79
	v_cvt_pk_bf16_f32 v66, v72, v73
	v_cvt_pk_bf16_f32 v67, v74, v75
	ds_read_b128 v[180:183], v209 offset:59392
	s_waitcnt lgkmcnt(6)
	v_mfma_f32_16x16x32_bf16 v[88:91], v[234:237], v[108:111], v[88:91]
	v_cvt_pk_bf16_f32 v70, v76, v77
	v_cvt_pk_bf16_f32 v71, v78, v79
	v_mfma_f32_16x16x32_bf16 v[92:95], v[234:237], v[124:127], v[92:95]
	ds_read_b128 v[230:233], v209 offset:61440
	s_waitcnt lgkmcnt(6)
	v_mfma_f32_16x16x32_bf16 v[0:3], v[160:163], v[64:67], v[0:3]
	v_exp_f32_e32 v80, v80
	v_exp_f32_e32 v81, v81
	v_exp_f32_e32 v82, v82
	v_mfma_f32_16x16x32_bf16 v[4:7], v[160:163], v[68:71], v[4:7]
	v_exp_f32_e32 v83, v83
	v_exp_f32_e32 v84, v84
	v_exp_f32_e32 v85, v85
	ds_read_b128 v[234:237], v209 offset:63488
	s_waitcnt lgkmcnt(6)
	v_mfma_f32_16x16x32_bf16 v[8:11], v[164:167], v[64:67], v[8:11]
	v_exp_f32_e32 v86, v86
	v_exp_f32_e32 v87, v87
	v_add_f32_e32 v194, v194, v80
	v_mfma_f32_16x16x32_bf16 v[12:15], v[164:167], v[68:71], v[12:15]
	v_add_f32_e32 v194, v194, v81
	v_add_f32_e32 v194, v194, v82
	v_add_f32_e32 v194, v194, v83
	ds_read_b128 v[160:163], v210 offset:49152
	s_waitcnt lgkmcnt(6)
	v_mfma_f32_16x16x32_bf16 v[16:19], v[168:171], v[64:67], v[16:19]
	v_add_f32_e32 v195, v195, v84
	v_add_f32_e32 v195, v195, v85
	v_add_f32_e32 v195, v195, v86
	v_mfma_f32_16x16x32_bf16 v[20:23], v[168:171], v[68:71], v[20:23]
	v_add_f32_e32 v195, v195, v87
	v_cvt_pk_bf16_f32 v80, v80, v81
	v_cvt_pk_bf16_f32 v81, v82, v83
	ds_read_b128 v[164:167], v210 offset:51200
	s_waitcnt lgkmcnt(6)
	v_mfma_f32_16x16x32_bf16 v[24:27], v[172:175], v[64:67], v[24:27]
	v_cvt_pk_bf16_f32 v84, v84, v85
	v_cvt_pk_bf16_f32 v85, v86, v87
	v_mfma_f32_16x16x32_bf16 v[28:31], v[172:175], v[68:71], v[28:31]
	ds_read_b128 v[168:171], v210 offset:53248
	s_waitcnt lgkmcnt(6)
	v_mfma_f32_16x16x32_bf16 v[32:35], v[176:179], v[64:67], v[32:35]
	v_exp_f32_e32 v88, v88
	v_exp_f32_e32 v89, v89
	v_exp_f32_e32 v90, v90
	v_mfma_f32_16x16x32_bf16 v[36:39], v[176:179], v[68:71], v[36:39]
	v_exp_f32_e32 v91, v91
	v_exp_f32_e32 v92, v92
	v_exp_f32_e32 v93, v93
	ds_read_b128 v[172:175], v210 offset:55296
	s_add_u32 s10, s10, 0x200
	s_addc_u32 s11, s11, 0
	s_add_u32 s12, s12, 0x40000
	s_addc_u32 s13, s13, 0
	s_add_i32 s4, s4, 4
	s_cmpk_lt_u32 s4, 0x104
	s_cselect_b64 s[6:7], -1, 0
	s_and_b64 s[6:7], s[0:1], s[6:7]
	s_and_b64 vcc, exec, s[6:7]
	s_waitcnt lgkmcnt(6)
	v_mfma_f32_16x16x32_bf16 v[40:43], v[180:183], v[64:67], v[40:43]
	v_exp_f32_e32 v94, v94
	v_exp_f32_e32 v95, v95
	v_add_f32_e32 v194, v194, v88
	v_mfma_f32_16x16x32_bf16 v[44:47], v[180:183], v[68:71], v[44:47]
	v_add_f32_e32 v194, v194, v89
	v_add_f32_e32 v194, v194, v90
	v_add_f32_e32 v194, v194, v91
	ds_read_b128 v[176:179], v210 offset:57344
	s_waitcnt lgkmcnt(6)
	v_mfma_f32_16x16x32_bf16 v[48:51], v[230:233], v[64:67], v[48:51]
	v_add_f32_e32 v195, v195, v92
	v_add_f32_e32 v195, v195, v93
	v_add_f32_e32 v195, v195, v94
	v_mfma_f32_16x16x32_bf16 v[52:55], v[230:233], v[68:71], v[52:55]
	v_add_f32_e32 v195, v195, v95
	v_cvt_pk_bf16_f32 v82, v88, v89
	v_cvt_pk_bf16_f32 v83, v90, v91
	ds_read_b128 v[180:183], v210 offset:59392
	s_waitcnt lgkmcnt(6)
	v_mfma_f32_16x16x32_bf16 v[56:59], v[234:237], v[64:67], v[56:59]
	v_cvt_pk_bf16_f32 v86, v92, v93
	v_cvt_pk_bf16_f32 v87, v94, v95
	v_mfma_f32_16x16x32_bf16 v[60:63], v[234:237], v[68:71], v[60:63]
	ds_read_b128 v[230:233], v210 offset:61440
	s_waitcnt lgkmcnt(6)
	v_mfma_f32_16x16x32_bf16 v[0:3], v[160:163], v[80:83], v[0:3]
	v_mfma_f32_16x16x32_bf16 v[4:7], v[160:163], v[84:87], v[4:7]
	ds_read_b128 v[234:237], v210 offset:63488
	s_waitcnt lgkmcnt(6)
	v_mfma_f32_16x16x32_bf16 v[8:11], v[164:167], v[80:83], v[8:11]
	v_mfma_f32_16x16x32_bf16 v[12:15], v[164:167], v[84:87], v[12:15]
	s_waitcnt lgkmcnt(5)
	v_mfma_f32_16x16x32_bf16 v[16:19], v[168:171], v[80:83], v[16:19]
	v_mfma_f32_16x16x32_bf16 v[20:23], v[168:171], v[84:87], v[20:23]
	s_waitcnt lgkmcnt(4)
	v_mfma_f32_16x16x32_bf16 v[24:27], v[172:175], v[80:83], v[24:27]
	v_mfma_f32_16x16x32_bf16 v[28:31], v[172:175], v[84:87], v[28:31]
	s_waitcnt lgkmcnt(3)
	v_mfma_f32_16x16x32_bf16 v[32:35], v[176:179], v[80:83], v[32:35]
	v_mfma_f32_16x16x32_bf16 v[36:39], v[176:179], v[84:87], v[36:39]
	s_waitcnt lgkmcnt(2)
	v_mfma_f32_16x16x32_bf16 v[40:43], v[180:183], v[80:83], v[40:43]
	v_mfma_f32_16x16x32_bf16 v[44:47], v[180:183], v[84:87], v[44:47]
	s_waitcnt lgkmcnt(1)
	v_mfma_f32_16x16x32_bf16 v[48:51], v[230:233], v[80:83], v[48:51]
	v_mfma_f32_16x16x32_bf16 v[52:55], v[230:233], v[84:87], v[52:55]
	s_waitcnt lgkmcnt(0)
	v_mfma_f32_16x16x32_bf16 v[56:59], v[234:237], v[80:83], v[56:59]
	v_mfma_f32_16x16x32_bf16 v[60:63], v[234:237], v[84:87], v[60:63]
	s_cbranch_vccnz .LBB0_734
	s_waitcnt vmcnt(0)
	s_nop 7
	s_nop 7
	ds_swizzle_b32 v64, v194 offset:swizzle(SWAP,16)
	s_waitcnt lgkmcnt(0)
	v_add_f32_e32 v194, v194, v64
	v_mov_b32_e32 v65, v194
	s_nop 1
	v_permlane32_swap_b32_e32 v194, v65
	v_add_f32_e32 v194, v194, v65
	s_nop 0
	v_rcp_f32_e32 v66, v194
	ds_swizzle_b32 v64, v195 offset:swizzle(SWAP,16)
	s_waitcnt lgkmcnt(0)
	v_add_f32_e32 v195, v195, v64
	v_mov_b32_e32 v65, v195
	s_nop 1
	v_permlane32_swap_b32_e32 v195, v65
	v_add_f32_e32 v195, v195, v65
	s_nop 0
	v_rcp_f32_e32 v67, v195
	v_readlane_b32 s100, v250, 8
	v_mbcnt_lo_u32_b32 v68, -1, 0
	v_mbcnt_hi_u32_b32 v68, -1, v68
	v_and_b32_e32 v69, 15, v68
	v_lshrrev_b32_e32 v70, 4, v68
	s_lshr_b32 s101, s100, 1
	v_add_u32_e32 v69, s101, v69
	v_lshlrev_b32_e32 v69, 12, v69
	v_and_b32_e32 v71, 1, v70
	v_lshlrev_b32_e32 v71, 5, v71
	v_and_b32_e32 v70, 2, v70
	v_lshl_add_u32 v71, v70, 3, v71
	v_add_u32_e32 v70, v69, v71
	v_add_u32_e32 v71, 0x10000, v70
	v_mul_f32_e32 v0, v0, v66
	v_mul_f32_e32 v1, v1, v66
	v_mul_f32_e32 v2, v2, v66
	v_mul_f32_e32 v3, v3, v66
	v_mul_f32_e32 v8, v8, v66
	v_mul_f32_e32 v9, v9, v66
	v_mul_f32_e32 v10, v10, v66
	v_mul_f32_e32 v11, v11, v66
	v_cvt_pk_bf16_f32 v72, v0, v1
	v_cvt_pk_bf16_f32 v73, v2, v3
	v_cvt_pk_bf16_f32 v74, v8, v9
	v_cvt_pk_bf16_f32 v75, v10, v11
	s_nop 1
	v_permlane16_swap_b32_e32 v72, v74
	v_permlane16_swap_b32_e32 v73, v75
	s_nop 1
	global_store_dwordx4 v70, v[72:75], s[58:59] offset:0
	v_mul_f32_e32 v16, v16, v66
	v_mul_f32_e32 v17, v17, v66
	v_mul_f32_e32 v18, v18, v66
	v_mul_f32_e32 v19, v19, v66
	v_mul_f32_e32 v24, v24, v66
	v_mul_f32_e32 v25, v25, v66
	v_mul_f32_e32 v26, v26, v66
	v_mul_f32_e32 v27, v27, v66
	v_cvt_pk_bf16_f32 v76, v16, v17
	v_cvt_pk_bf16_f32 v77, v18, v19
	v_cvt_pk_bf16_f32 v78, v24, v25
	v_cvt_pk_bf16_f32 v79, v26, v27
	s_nop 1
	v_permlane16_swap_b32_e32 v76, v78
	v_permlane16_swap_b32_e32 v77, v79
	s_nop 1
	global_store_dwordx4 v70, v[76:79], s[58:59] offset:64
	v_mul_f32_e32 v32, v32, v66
	v_mul_f32_e32 v33, v33, v66
	v_mul_f32_e32 v34, v34, v66
	v_mul_f32_e32 v35, v35, v66
	v_mul_f32_e32 v40, v40, v66
	v_mul_f32_e32 v41, v41, v66
	v_mul_f32_e32 v42, v42, v66
	v_mul_f32_e32 v43, v43, v66
	v_cvt_pk_bf16_f32 v80, v32, v33
	v_cvt_pk_bf16_f32 v81, v34, v35
	v_cvt_pk_bf16_f32 v82, v40, v41
	v_cvt_pk_bf16_f32 v83, v42, v43
	s_nop 1
	v_permlane16_swap_b32_e32 v80, v82
	v_permlane16_swap_b32_e32 v81, v83
	s_nop 1
	global_store_dwordx4 v70, v[80:83], s[58:59] offset:128
	v_mul_f32_e32 v48, v48, v66
	v_mul_f32_e32 v49, v49, v66
	v_mul_f32_e32 v50, v50, v66
	v_mul_f32_e32 v51, v51, v66
	v_mul_f32_e32 v56, v56, v66
	v_mul_f32_e32 v57, v57, v66
	v_mul_f32_e32 v58, v58, v66
	v_mul_f32_e32 v59, v59, v66
	v_cvt_pk_bf16_f32 v84, v48, v49
	v_cvt_pk_bf16_f32 v85, v50, v51
	v_cvt_pk_bf16_f32 v86, v56, v57
	v_cvt_pk_bf16_f32 v87, v58, v59
	s_nop 1
	v_permlane16_swap_b32_e32 v84, v86
	v_permlane16_swap_b32_e32 v85, v87
	s_nop 1
	global_store_dwordx4 v70, v[84:87], s[58:59] offset:192
	v_mul_f32_e32 v4, v4, v67
	v_mul_f32_e32 v5, v5, v67
	v_mul_f32_e32 v6, v6, v67
	v_mul_f32_e32 v7, v7, v67
	v_mul_f32_e32 v12, v12, v67
	v_mul_f32_e32 v13, v13, v67
	v_mul_f32_e32 v14, v14, v67
	v_mul_f32_e32 v15, v15, v67
	v_cvt_pk_bf16_f32 v88, v4, v5
	v_cvt_pk_bf16_f32 v89, v6, v7
	v_cvt_pk_bf16_f32 v90, v12, v13
	v_cvt_pk_bf16_f32 v91, v14, v15
	s_nop 1
	v_permlane16_swap_b32_e32 v88, v90
	v_permlane16_swap_b32_e32 v89, v91
	s_nop 1
	global_store_dwordx4 v71, v[88:91], s[58:59] offset:0
	v_mul_f32_e32 v20, v20, v67
	v_mul_f32_e32 v21, v21, v67
	v_mul_f32_e32 v22, v22, v67
	v_mul_f32_e32 v23, v23, v67
	v_mul_f32_e32 v28, v28, v67
	v_mul_f32_e32 v29, v29, v67
	v_mul_f32_e32 v30, v30, v67
	v_mul_f32_e32 v31, v31, v67
	v_cvt_pk_bf16_f32 v92, v20, v21
	v_cvt_pk_bf16_f32 v93, v22, v23
	v_cvt_pk_bf16_f32 v94, v28, v29
	v_cvt_pk_bf16_f32 v95, v30, v31
	s_nop 1
	v_permlane16_swap_b32_e32 v92, v94
	v_permlane16_swap_b32_e32 v93, v95
	s_nop 1
	global_store_dwordx4 v71, v[92:95], s[58:59] offset:64
	v_mul_f32_e32 v36, v36, v67
	v_mul_f32_e32 v37, v37, v67
	v_mul_f32_e32 v38, v38, v67
	v_mul_f32_e32 v39, v39, v67
	v_mul_f32_e32 v44, v44, v67
	v_mul_f32_e32 v45, v45, v67
	v_mul_f32_e32 v46, v46, v67
	v_mul_f32_e32 v47, v47, v67
	v_cvt_pk_bf16_f32 v72, v36, v37
	v_cvt_pk_bf16_f32 v73, v38, v39
	v_cvt_pk_bf16_f32 v74, v44, v45
	v_cvt_pk_bf16_f32 v75, v46, v47
	s_nop 1
	v_permlane16_swap_b32_e32 v72, v74
	v_permlane16_swap_b32_e32 v73, v75
	s_nop 1
	global_store_dwordx4 v71, v[72:75], s[58:59] offset:128
	v_mul_f32_e32 v52, v52, v67
	v_mul_f32_e32 v53, v53, v67
	v_mul_f32_e32 v54, v54, v67
	v_mul_f32_e32 v55, v55, v67
	v_mul_f32_e32 v60, v60, v67
	v_mul_f32_e32 v61, v61, v67
	v_mul_f32_e32 v62, v62, v67
	v_mul_f32_e32 v63, v63, v67
	v_cvt_pk_bf16_f32 v76, v52, v53
	v_cvt_pk_bf16_f32 v77, v54, v55
	v_cvt_pk_bf16_f32 v78, v60, v61
	v_cvt_pk_bf16_f32 v79, v62, v63
	s_nop 1
	v_permlane16_swap_b32_e32 v76, v78
	v_permlane16_swap_b32_e32 v77, v79
	s_nop 1
	global_store_dwordx4 v71, v[76:79], s[58:59] offset:192
	s_barrier

	.amdhsa_kernel _Z6mk_fwd4Args
		.amdhsa_group_segment_fixed_size 0
		.amdhsa_private_segment_fixed_size 0
		.amdhsa_kernarg_size 464
		.amdhsa_user_sgpr_count 2
		.amdhsa_user_sgpr_dispatch_ptr 0
		.amdhsa_user_sgpr_queue_ptr 0
		.amdhsa_user_sgpr_kernarg_segment_ptr 1
		.amdhsa_user_sgpr_dispatch_id 0
		.amdhsa_user_sgpr_kernarg_preload_length 0
		.amdhsa_user_sgpr_kernarg_preload_offset 0
		.amdhsa_user_sgpr_private_segment_size 0
		.amdhsa_uses_dynamic_stack 0
		.amdhsa_enable_private_segment 0
		.amdhsa_system_sgpr_workgroup_id_x 1
		.amdhsa_system_sgpr_workgroup_id_y 0
		.amdhsa_system_sgpr_workgroup_id_z 0
		.amdhsa_system_sgpr_workgroup_info 0
		.amdhsa_system_vgpr_workitem_id 0
		.amdhsa_next_free_vgpr 256
		.amdhsa_next_free_sgpr 102
		.amdhsa_accum_offset 256
		.amdhsa_reserve_vcc 1
		.amdhsa_float_round_mode_32 0
		.amdhsa_float_round_mode_16_64 0
		.amdhsa_float_denorm_mode_32 3
		.amdhsa_float_denorm_mode_16_64 3
		.amdhsa_dx10_clamp 1
		.amdhsa_ieee_mode 1
		.amdhsa_fp16_overflow 0
		.amdhsa_tg_split 0
		.amdhsa_exception_fp_ieee_invalid_op 0
		.amdhsa_exception_fp_denorm_src 0
		.amdhsa_exception_fp_ieee_div_zero 0
		.amdhsa_exception_fp_ieee_overflow 0
		.amdhsa_exception_fp_ieee_underflow 0
		.amdhsa_exception_fp_ieee_inexact 0
		.amdhsa_exception_int_div_zero 0
	.end_amdhsa_kernel

amdhsa.kernels:
  - .agpr_count:     0
    .args:
      - .offset:         0
        .size:           208
        .value_kind:     by_value
      - .offset:         208
        .size:           4
        .value_kind:     hidden_block_count_x
      - .offset:         212
        .size:           4
        .value_kind:     hidden_block_count_y
      - .offset:         216
        .size:           4
        .value_kind:     hidden_block_count_z
      - .offset:         220
        .size:           2
        .value_kind:     hidden_group_size_x
      - .offset:         222
        .size:           2
        .value_kind:     hidden_group_size_y
      - .offset:         224
        .size:           2
        .value_kind:     hidden_group_size_z
      - .offset:         226
        .size:           2
        .value_kind:     hidden_remainder_x
      - .offset:         228
        .size:           2
        .value_kind:     hidden_remainder_y
      - .offset:         230
        .size:           2
        .value_kind:     hidden_remainder_z
      - .offset:         248
        .size:           8
        .value_kind:     hidden_global_offset_x
      - .offset:         256
        .size:           8
        .value_kind:     hidden_global_offset_y
      - .offset:         264
        .size:           8
        .value_kind:     hidden_global_offset_z
      - .offset:         272
        .size:           2
        .value_kind:     hidden_grid_dims
      - .offset:         328
        .size:           4
        .value_kind:     hidden_dynamic_lds_size
    .group_segment_fixed_size: 0
    .kernarg_segment_align: 8
    .kernarg_segment_size: 464
    .language:       OpenCL C
    .language_version:
      - 2
      - 0
    .max_flat_workgroup_size: 512
    .name:           _Z6mk_fwd4Args
    .private_segment_fixed_size: 0
    .sgpr_count:     108
    .sgpr_spill_count: 449
    .symbol:         _Z6mk_fwd4Args.kd
    .uniform_work_group_size: 1
    .uses_dynamic_stack: false
    .vgpr_count:     256
    .vgpr_spill_count: 0
    .wavefront_size: 64
